# speedup vs baseline: 1.0979x; 1.0199x over previous
_Z6scan_kPKDF16_S0_S0_S0_PKfPf:
	s_load_dwordx8 s[4:11], s[0:1], 0x0
	s_load_dwordx4 s[12:15], s[0:1], 0x20
	v_and_b32_e32 v1, 63, v0
	v_lshrrev_b32_e32 v2, 6, v0
	s_nop 1
	v_readfirstlane_b32 s16, v2
	s_lshr_b32 s17, s2, 7
	s_and_b32 s18, s2, 127
	s_lshl_b32 s18, s18, 2
	s_add_u32 s18, s18, s16
	s_lshl_b32 s19, s17, 9
	s_add_u32 s19, s19, s18
	s_mul_i32 s28, s16, 4608
	s_add_u32 s28, s28, 67584
	s_lshl_b32 s32, s16, 10
	s_add_u32 s33, s32, 0x1000
	s_add_u32 s34, s32, 0x2000
	s_add_u32 s35, s32, 0x3000
	s_mov_b32 s46, 0x200
	s_mov_b32 s47, 0
	s_mov_b32 s40, 0
	v_lshlrev_b32_e32 v2, 4, v1
	v_add_u32_e32 v3, 0x1000, v2
	v_add_u32_e32 v4, 0x2000, v2
	v_add_u32_e32 v5, 0x3000, v2
	v_lshlrev_b32_e32 v6, 2, v1
	v_lshlrev_b32_e32 v7, 1, v1
	v_and_b32_e32 v20, 7, v1
	v_lshlrev_b32_e32 v20, 1, v20
	v_add_u32_e32 v8, v2, v20
	v_add_u32_e32 v8, s28, v8
	v_and_b32_e32 v20, 3, v1
	v_bfe_u32 v21, v1, 3, 2
	v_lshl_add_u32 v20, v21, 2, v20
	v_lshrrev_b32_e32 v21, 5, v1
	v_bfe_u32 v22, v1, 2, 1
	v_bfe_u32 v23, v1, 4, 1
	v_cmp_eq_u32_e64 s[48:49], v21, v22
	v_cmp_eq_u32_e64 s[50:51], 0, v23
	s_nop 1
	s_and_b64 s[52:53], s[48:49], s[50:51]
	s_andn2_b64 s[54:55], s[48:49], s[50:51]
	v_mov_b32_e32 v24, 65536
	v_lshlrev_b32_e32 v25, 1, v20
	v_add_u32_e32 v25, s28, v25
	v_add_u32_e32 v26, 0x100, v25
	s_nop 1
	v_cndmask_b32_e64 v9, v24, v25, s[48:49]
	v_cndmask_b32_e64 v10, v24, v26, s[48:49]
	v_lshlrev_b32_e32 v25, 4, v20
	v_add_u32_e32 v25, s28, v25
	v_add_u32_e32 v25, 0x200, v25
	v_add_u32_e32 v26, 0x800, v25
	v_cndmask_b32_e64 v11, v24, v25, s[48:49]
	v_cndmask_b32_e64 v13, v24, v26, s[48:49]
	v_mov_b32_e32 v15, 1.0
	v_and_b32_e32 v89, 15, v1
	v_cmp_eq_u32_e64 s[42:43], 0, v89
	s_waitcnt lgkmcnt(0)
	s_lshl_b32 s30, s19, 13
	s_add_u32 s24, s4, s30
	s_addc_u32 s25, s5, 0
	s_add_u32 s26, s6, s30
	s_addc_u32 s27, s7, 0
	s_lshl_b32 s30, s17, 19
	s_add_u32 s30, s30, s32
	s_add_u32 s20, s8, s30
	s_addc_u32 s21, s9, 0
	s_add_u32 s22, s10, s30
	s_addc_u32 s23, s11, 0
	s_lshl_b32 s30, s18, 8
	s_add_u32 s12, s12, s30
	s_addc_u32 s13, s13, 0
	global_load_dword v90, v6, s[12:13]
	global_load_ushort v18, v7, s[26:27]
	global_load_ushort v19, v7, s[26:27] offset:128
	s_lshl_b32 s30, s19, 14
	s_add_u32 s14, s14, s30
	s_addc_u32 s15, s15, 0
	v_and_b32_e32 v30, 48, v1
	v_mov_b32_e32 v31, 0
	v_lshl_add_u64 v[16:17], s[14:15], 0, v[30:31]
	v_mov_b32_e32 v36, 0
	v_mov_b32_e32 v37, 0
	v_mov_b32_e32 v38, 0
	v_mov_b32_e32 v39, 0
	v_add_u32_e32 v29, 65536, v2
	ds_write_b128 v29, v[36:39]
	ds_write_b128 v29, v[36:39] offset:1024
	v_add_u32_e32 v29, s28, v2
	ds_write_b128 v29, v[36:39] offset:512
	ds_write_b128 v29, v[36:39] offset:1536
	ds_write_b128 v29, v[36:39] offset:2560
	ds_write_b128 v29, v[36:39] offset:3584
	s_mov_b32 m0, s32
	s_nop 0
	global_load_lds_dwordx4 v2, s[20:21]
	s_add_i32 m0, s32, 32768
	s_nop 0
	global_load_lds_dwordx4 v2, s[22:23]
	s_mov_b32 m0, s33
	s_nop 0
	global_load_lds_dwordx4 v3, s[20:21]
	s_add_i32 m0, s33, 32768
	s_nop 0
	global_load_lds_dwordx4 v3, s[22:23]
	s_mov_b32 m0, s34
	s_nop 0
	global_load_lds_dwordx4 v4, s[20:21]
	s_add_i32 m0, s34, 32768
	s_nop 0
	global_load_lds_dwordx4 v4, s[22:23]
	s_mov_b32 m0, s35
	s_nop 0
	global_load_lds_dwordx4 v5, s[20:21]
	s_add_i32 m0, s35, 32768
	s_nop 0
	global_load_lds_dwordx4 v5, s[22:23]
	s_mov_b32 m0, s28
	s_nop 0
	global_load_lds_dword v6, s[24:25]
	s_add_u32 s20, s20, 0x4000
	s_addc_u32 s21, s21, 0
	s_add_u32 s22, s22, 0x4000
	s_addc_u32 s23, s23, 0
	s_add_u32 s24, s24, 0x100
	s_addc_u32 s25, s25, 0
	s_add_i32 m0, s32, 16384
	s_nop 0
	global_load_lds_dwordx4 v2, s[20:21]
	s_add_i32 m0, s32, 49152
	s_nop 0
	global_load_lds_dwordx4 v2, s[22:23]
	s_add_i32 m0, s33, 16384
	s_nop 0
	global_load_lds_dwordx4 v3, s[20:21]
	s_add_i32 m0, s33, 49152
	s_nop 0
	global_load_lds_dwordx4 v3, s[22:23]
	s_add_i32 m0, s34, 16384
	s_nop 0
	global_load_lds_dwordx4 v4, s[20:21]
	s_add_i32 m0, s34, 49152
	s_nop 0
	global_load_lds_dwordx4 v4, s[22:23]
	s_add_i32 m0, s35, 16384
	s_nop 0
	global_load_lds_dwordx4 v5, s[20:21]
	s_add_i32 m0, s35, 49152
	s_nop 0
	global_load_lds_dwordx4 v5, s[22:23]
	s_add_i32 m0, s28, 0x100
	s_nop 0
	global_load_lds_dword v6, s[24:25]
	s_add_u32 s20, s20, 0x4000
	s_addc_u32 s21, s21, 0
	s_add_u32 s22, s22, 0x4000
	s_addc_u32 s23, s23, 0
	s_add_u32 s24, s24, 0x100
	s_addc_u32 s25, s25, 0
	s_mov_b32 s3, 0x3fb8aa3b
	s_waitcnt vmcnt(20)
	v_mul_f32_e32 v91, 0x3fb8aa3b, v90
	v_fma_f32 v92, v90, s3, -v91
	v_rndne_f32_e32 v93, v91
	v_fmamk_f32 v92, v90, 0x32a5705f, v92
	v_sub_f32_e32 v91, v91, v93
	v_add_f32_e32 v91, v91, v92
	v_exp_f32_e32 v91, v91
	v_cvt_i32_f32_e32 v92, v93
	s_mov_b32 s3, 0xc2ce8ed0
	v_cmp_ngt_f32_e32 vcc, s3, v90
	s_mov_b32 s3, 0x42b17218
	v_ldexp_f32 v91, v91, v92
	v_cndmask_b32_e32 v91, 0, v91, vcc
	v_mov_b32_e32 v92, 0x7f800000
	v_cmp_nlt_f32_e32 vcc, s3, v90
	s_mov_b32 s3, 0xbfb8aa3b
	s_nop 1
	v_cndmask_b32_e32 v90, v92, v91, vcc
	v_mov_b32_e32 v93, 0
	s_nop 0
	v_fma_mixlo_f16 v93, v90, s3, 0
	v_and_b32_e32 v28, 0xffff, v93
	v_mov_b32_e32 v29, 0
	v_mov_b32_e32 v30, 0
	v_mov_b32_e32 v31, 0
	v_mov_b32_e32 v32, 0
	v_mov_b32_e32 v33, 0
	v_mov_b32_e32 v34, 0
	v_mov_b32_e32 v35, 0
	v_mov_b32_e32 v94, 0x1c00
	v_mov_b32_e32 v95, 0x1c000000
	v_cmp_eq_u32_e32 vcc, 0, v89
	s_nop 1
	v_cndmask_b32_e32 v20, 0, v94, vcc
	v_cmp_eq_u32_e32 vcc, 1, v89
	s_nop 1
	v_cndmask_b32_e32 v20, v20, v95, vcc
	v_cmp_eq_u32_e32 vcc, 2, v89
	s_nop 1
	v_cndmask_b32_e32 v21, 0, v94, vcc
	v_cmp_eq_u32_e32 vcc, 3, v89
	s_nop 1
	v_cndmask_b32_e32 v21, v21, v95, vcc
	v_cmp_eq_u32_e32 vcc, 4, v89
	s_nop 1
	v_cndmask_b32_e32 v22, 0, v94, vcc
	v_cmp_eq_u32_e32 vcc, 5, v89
	s_nop 1
	v_cndmask_b32_e32 v22, v22, v95, vcc
	v_cmp_eq_u32_e32 vcc, 6, v89
	s_nop 1
	v_cndmask_b32_e32 v23, 0, v94, vcc
	v_cmp_eq_u32_e32 vcc, 7, v89
	s_nop 1
	v_cndmask_b32_e32 v23, v23, v95, vcc
	v_cmp_eq_u32_e32 vcc, 8, v89
	s_nop 1
	v_cndmask_b32_e32 v24, 0, v94, vcc
	v_cmp_eq_u32_e32 vcc, 9, v89
	s_nop 1
	v_cndmask_b32_e32 v24, v24, v95, vcc
	v_cmp_eq_u32_e32 vcc, 10, v89
	s_nop 1
	v_cndmask_b32_e32 v25, 0, v94, vcc
	v_cmp_eq_u32_e32 vcc, 11, v89
	s_nop 1
	v_cndmask_b32_e32 v25, v25, v95, vcc
	v_cmp_eq_u32_e32 vcc, 12, v89
	s_nop 1
	v_cndmask_b32_e32 v26, 0, v94, vcc
	v_cmp_eq_u32_e32 vcc, 13, v89
	s_nop 1
	v_cndmask_b32_e32 v26, v26, v95, vcc
	v_cmp_eq_u32_e32 vcc, 14, v89
	s_nop 1
	v_cndmask_b32_e32 v27, 0, v94, vcc
	v_cmp_eq_u32_e32 vcc, 15, v89
	s_nop 1
	v_cndmask_b32_e32 v27, v27, v95, vcc
	v_mov_b32_e32 v191, 0
	v_mov_b32_e32 v68, 0
	v_mov_b32_e32 v69, 0
	v_mov_b32_e32 v70, 0
	v_mov_b32_e32 v71, 0
	v_mov_b32_e32 v72, 0
	v_mov_b32_e32 v73, 0
	v_mov_b32_e32 v74, 0
	v_mov_b32_e32 v75, 0
	v_mov_b32_e32 v76, 0
	v_mov_b32_e32 v77, 0
	v_mov_b32_e32 v78, 0
	v_mov_b32_e32 v79, 0
	v_mov_b32_e32 v80, 0
	v_mov_b32_e32 v81, 0
	v_mov_b32_e32 v82, 0
	v_mov_b32_e32 v83, 0
	s_waitcnt vmcnt(18)
	ds_write_b16 v8, v18 offset:512
	ds_write_b16 v8, v19 offset:1536
	s_add_u32 s26, s26, 0x100
	s_addc_u32 s27, s27, 0
	global_load_ushort v18, v7, s[26:27]
	global_load_ushort v19, v7, s[26:27] offset:128
	s_add_u32 s26, s26, 0x100
	s_addc_u32 s27, s27, 0
	s_waitcnt vmcnt(0)
	s_waitcnt lgkmcnt(0)
	s_barrier
	ds_read_b128 v[52:55], v2 offset:32768
	ds_read_b128 v[56:59], v2 offset:33792
	ds_read_u16 v32, v9 offset:0
	ds_read_b128 v[36:39], v11 offset:0
	ds_read_b128 v[44:47], v2 offset:0
	ds_read_b128 v[48:51], v2 offset:1024
	s_waitcnt lgkmcnt(0)
	v_mfma_f32_32x32x16_f16 v[96:111], v[32:35], v[28:31], 0
	v_mfma_f32_32x32x16_f16 v[128:143], v[36:39], v[44:47], 0
	v_mfma_f32_32x32x16_f16 v[160:175], v[36:39], v[48:51], 0
	ds_read_u16 v32, v9 offset:32
	ds_read_b128 v[36:39], v11 offset:256
	ds_read_b128 v[44:47], v2 offset:2048
	ds_read_b128 v[48:51], v2 offset:3072
	s_nop 15
	s_nop 15
.Lscan_loop:
	v_exp_f32_e32 v96, v96
	v_exp_f32_e32 v97, v97
	v_mfma_f32_16x16x32_f16 v[80:83], v[72:75], v[24:27], v[80:83]
	ds_read_b128 v[60:63], v2 offset:34816
	s_waitcnt lgkmcnt(1)
	v_exp_f32_e32 v98, v98
	v_exp_f32_e32 v99, v99
	v_mfma_f32_32x32x16_f16 v[112:127], v[32:35], v[28:31], 0
	ds_read_u16 v32, v9 offset:64
	ds_read_b128 v[64:67], v2 offset:35840
	v_fmac_f32_e32 v128, v96, v191
	v_exp_f32_e32 v100, v100
	v_fmac_f32_e32 v129, v97, v128
	v_exp_f32_e32 v101, v101
	v_fmac_f32_e32 v130, v98, v129
	v_cvt_pkrtz_f16_f32 v68, v128, v129
	v_exp_f32_e32 v102, v102
	v_fmac_f32_e32 v131, v99, v130
	v_pk_mul_f16 v68, v52, v68
	v_exp_f32_e32 v103, v103
	v_mfma_f32_32x32x16_f16 v[144:159], v[36:39], v[44:47], 0
	ds_read_b128 v[44:47], v2 offset:4096
	v_fmac_f32_e32 v132, v100, v131
	v_cvt_pkrtz_f16_f32 v69, v130, v131
	v_exp_f32_e32 v104, v104
	v_fmac_f32_e32 v133, v101, v132
	v_pk_mul_f16 v69, v53, v69
	v_exp_f32_e32 v105, v105
	v_fmac_f32_e32 v134, v102, v133
	v_cvt_pkrtz_f16_f32 v70, v132, v133
	v_exp_f32_e32 v106, v106
	v_fmac_f32_e32 v135, v103, v134
	v_pk_mul_f16 v70, v54, v70
	v_exp_f32_e32 v107, v107
	v_mfma_f32_32x32x16_f16 v[176:191], v[36:39], v[48:51], 0
	ds_read_b128 v[36:39], v11 offset:512
	ds_read_b128 v[48:51], v2 offset:5120
	v_cvt_pkrtz_f16_f32 v71, v134, v135
	v_fmac_f32_e32 v168, v104, v135
	v_pk_mul_f16 v71, v55, v71
	v_exp_f32_e32 v108, v108
	v_fmac_f32_e32 v169, v105, v168
	v_mfma_f32_16x16x32_f16 v[76:79], v[68:71], v[20:23], 0
	v_cvt_pkrtz_f16_f32 v72, v168, v169
	v_exp_f32_e32 v109, v109
	v_fmac_f32_e32 v170, v106, v169
	v_pk_mul_f16 v72, v56, v72
	v_add_f32_e32 v84, v80, v81
	v_fmac_f32_e32 v171, v107, v170
	v_exp_f32_e32 v110, v110
	v_cvt_pkrtz_f16_f32 v73, v170, v171
	v_fmac_f32_e32 v172, v108, v171
	v_pk_mul_f16 v73, v57, v73
	v_add_f32_e32 v85, v82, v83
	v_fmac_f32_e32 v173, v109, v172
	v_exp_f32_e32 v111, v111
	v_cvt_pkrtz_f16_f32 v74, v172, v173
	v_fmac_f32_e32 v174, v110, v173
	v_add_f32_e32 v84, v84, v85
	v_fmac_f32_e32 v175, v111, v174
	v_pk_mul_f16 v74, v58, v74
	v_cvt_pkrtz_f16_f32 v75, v174, v175
	v_mfma_f32_16x16x4_f32 a[28:31], v84, v15, 0
	v_pk_mul_f16 v75, v59, v75
	v_exp_f32_e32 v112, v112
	v_exp_f32_e32 v113, v113
	v_mfma_f32_16x16x32_f16 v[76:79], v[72:75], v[24:27], v[76:79]
	ds_read_b128 v[52:55], v2 offset:36864
	s_waitcnt lgkmcnt(1)
	v_exp_f32_e32 v114, v114
	v_exp_f32_e32 v115, v115
	v_mfma_f32_32x32x16_f16 v[96:111], v[32:35], v[28:31], 0
	ds_read_u16 v32, v9 offset:96
	ds_read_b128 v[56:59], v2 offset:37888
	v_fmac_f32_e32 v144, v112, v175
	v_exp_f32_e32 v116, v116
	v_fmac_f32_e32 v145, v113, v144
	v_exp_f32_e32 v117, v117
	v_fmac_f32_e32 v146, v114, v145
	v_cvt_pkrtz_f16_f32 v68, v144, v145
	v_exp_f32_e32 v118, v118
	v_fmac_f32_e32 v147, v115, v146
	v_pk_mul_f16 v68, v60, v68
	v_exp_f32_e32 v119, v119
	v_mfma_f32_32x32x16_f16 v[128:143], v[36:39], v[44:47], 0
	ds_read_b128 v[44:47], v2 offset:6144
	v_fmac_f32_e32 v148, v116, v147
	v_cvt_pkrtz_f16_f32 v69, v146, v147
	v_exp_f32_e32 v120, v120
	v_fmac_f32_e32 v149, v117, v148
	v_pk_mul_f16 v69, v61, v69
	v_exp_f32_e32 v121, v121
	v_fmac_f32_e32 v150, v118, v149
	v_cvt_pkrtz_f16_f32 v70, v148, v149
	v_exp_f32_e32 v122, v122
	v_fmac_f32_e32 v151, v119, v150
	v_pk_mul_f16 v70, v62, v70
	v_exp_f32_e32 v123, v123
	v_mfma_f32_32x32x16_f16 v[160:175], v[36:39], v[48:51], 0
	ds_read_b128 v[36:39], v11 offset:768
	ds_read_b128 v[48:51], v2 offset:7168
	v_cvt_pkrtz_f16_f32 v71, v150, v151
	v_fmac_f32_e32 v184, v120, v151
	v_pk_mul_f16 v71, v63, v71
	v_exp_f32_e32 v124, v124
	v_fmac_f32_e32 v185, v121, v184
	v_mfma_f32_16x16x32_f16 v[80:83], v[68:71], v[20:23], 0
	v_cvt_pkrtz_f16_f32 v72, v184, v185
	v_exp_f32_e32 v125, v125
	v_fmac_f32_e32 v186, v122, v185
	v_pk_mul_f16 v72, v64, v72
	v_add_f32_e32 v84, v76, v77
	v_fmac_f32_e32 v187, v123, v186
	v_exp_f32_e32 v126, v126
	v_cvt_pkrtz_f16_f32 v73, v186, v187
	v_fmac_f32_e32 v188, v124, v187
	v_pk_mul_f16 v73, v65, v73
	v_add_f32_e32 v85, v78, v79
	v_fmac_f32_e32 v189, v125, v188
	v_exp_f32_e32 v127, v127
	v_cvt_pkrtz_f16_f32 v74, v188, v189
	v_fmac_f32_e32 v190, v126, v189
	v_add_f32_e32 v84, v84, v85
	v_fmac_f32_e32 v191, v127, v190
	v_pk_mul_f16 v74, v66, v74
	v_cvt_pkrtz_f16_f32 v75, v190, v191
	v_mfma_f32_16x16x4_f32 a[0:3], v84, v15, 0
	v_pk_mul_f16 v75, v67, v75
	v_exp_f32_e32 v96, v96
	v_exp_f32_e32 v97, v97
	v_mfma_f32_16x16x32_f16 v[80:83], v[72:75], v[24:27], v[80:83]
	ds_read_b128 v[60:63], v2 offset:38912
	s_waitcnt lgkmcnt(1)
	v_exp_f32_e32 v98, v98
	v_exp_f32_e32 v99, v99
	v_mfma_f32_32x32x16_f16 v[112:127], v[32:35], v[28:31], 0
	ds_read_u16 v32, v9 offset:128
	ds_read_b128 v[64:67], v2 offset:39936
	v_fmac_f32_e32 v128, v96, v191
	v_exp_f32_e32 v100, v100
	v_fmac_f32_e32 v129, v97, v128
	v_exp_f32_e32 v101, v101
	v_fmac_f32_e32 v130, v98, v129
	v_cvt_pkrtz_f16_f32 v68, v128, v129
	v_exp_f32_e32 v102, v102
	v_fmac_f32_e32 v131, v99, v130
	v_pk_mul_f16 v68, v52, v68
	v_exp_f32_e32 v103, v103
	v_mfma_f32_32x32x16_f16 v[144:159], v[36:39], v[44:47], 0
	ds_read_b128 v[44:47], v2 offset:8192
	v_fmac_f32_e32 v132, v100, v131
	v_cvt_pkrtz_f16_f32 v69, v130, v131
	v_exp_f32_e32 v104, v104
	v_fmac_f32_e32 v133, v101, v132
	v_pk_mul_f16 v69, v53, v69
	v_exp_f32_e32 v105, v105
	v_fmac_f32_e32 v134, v102, v133
	v_cvt_pkrtz_f16_f32 v70, v132, v133
	v_exp_f32_e32 v106, v106
	v_fmac_f32_e32 v135, v103, v134
	v_pk_mul_f16 v70, v54, v70
	v_exp_f32_e32 v107, v107
	v_mfma_f32_32x32x16_f16 v[176:191], v[36:39], v[48:51], 0
	ds_read_b128 v[36:39], v11 offset:1024
	ds_read_b128 v[48:51], v2 offset:9216
	v_cvt_pkrtz_f16_f32 v71, v134, v135
	v_fmac_f32_e32 v168, v104, v135
	v_pk_mul_f16 v71, v55, v71
	v_exp_f32_e32 v108, v108
	v_fmac_f32_e32 v169, v105, v168
	v_mfma_f32_16x16x32_f16 v[76:79], v[68:71], v[20:23], 0
	v_cvt_pkrtz_f16_f32 v72, v168, v169
	v_exp_f32_e32 v109, v109
	v_fmac_f32_e32 v170, v106, v169
	v_pk_mul_f16 v72, v56, v72
	v_add_f32_e32 v84, v80, v81
	v_fmac_f32_e32 v171, v107, v170
	v_exp_f32_e32 v110, v110
	v_cvt_pkrtz_f16_f32 v73, v170, v171
	v_fmac_f32_e32 v172, v108, v171
	v_pk_mul_f16 v73, v57, v73
	v_add_f32_e32 v85, v82, v83
	v_fmac_f32_e32 v173, v109, v172
	v_exp_f32_e32 v111, v111
	v_cvt_pkrtz_f16_f32 v74, v172, v173
	v_fmac_f32_e32 v174, v110, v173
	v_add_f32_e32 v84, v84, v85
	v_fmac_f32_e32 v175, v111, v174
	v_pk_mul_f16 v74, v58, v74
	v_cvt_pkrtz_f16_f32 v75, v174, v175
	v_mfma_f32_16x16x4_f32 a[4:7], v84, v15, 0
	v_pk_mul_f16 v75, v59, v75
	v_exp_f32_e32 v112, v112
	v_exp_f32_e32 v113, v113
	v_mfma_f32_16x16x32_f16 v[76:79], v[72:75], v[24:27], v[76:79]
	ds_read_b128 v[52:55], v2 offset:40960
	s_waitcnt lgkmcnt(1)
	v_exp_f32_e32 v114, v114
	v_exp_f32_e32 v115, v115
	v_mfma_f32_32x32x16_f16 v[96:111], v[32:35], v[28:31], 0
	ds_read_u16 v32, v9 offset:160
	ds_read_b128 v[56:59], v2 offset:41984
	v_fmac_f32_e32 v144, v112, v175
	v_exp_f32_e32 v116, v116
	v_fmac_f32_e32 v145, v113, v144
	v_exp_f32_e32 v117, v117
	v_fmac_f32_e32 v146, v114, v145
	v_cvt_pkrtz_f16_f32 v68, v144, v145
	v_exp_f32_e32 v118, v118
	v_fmac_f32_e32 v147, v115, v146
	v_pk_mul_f16 v68, v60, v68
	v_exp_f32_e32 v119, v119
	v_mfma_f32_32x32x16_f16 v[128:143], v[36:39], v[44:47], 0
	ds_read_b128 v[44:47], v2 offset:10240
	v_fmac_f32_e32 v148, v116, v147
	v_cvt_pkrtz_f16_f32 v69, v146, v147
	v_exp_f32_e32 v120, v120
	v_fmac_f32_e32 v149, v117, v148
	v_pk_mul_f16 v69, v61, v69
	v_exp_f32_e32 v121, v121
	v_fmac_f32_e32 v150, v118, v149
	v_cvt_pkrtz_f16_f32 v70, v148, v149
	v_exp_f32_e32 v122, v122
	v_fmac_f32_e32 v151, v119, v150
	v_pk_mul_f16 v70, v62, v70
	v_exp_f32_e32 v123, v123
	v_mfma_f32_32x32x16_f16 v[160:175], v[36:39], v[48:51], 0
	ds_read_b128 v[36:39], v11 offset:1280
	ds_read_b128 v[48:51], v2 offset:11264
	v_cvt_pkrtz_f16_f32 v71, v150, v151
	v_fmac_f32_e32 v184, v120, v151
	v_pk_mul_f16 v71, v63, v71
	v_exp_f32_e32 v124, v124
	v_fmac_f32_e32 v185, v121, v184
	v_mfma_f32_16x16x32_f16 v[80:83], v[68:71], v[20:23], 0
	v_cvt_pkrtz_f16_f32 v72, v184, v185
	v_exp_f32_e32 v125, v125
	v_fmac_f32_e32 v186, v122, v185
	v_pk_mul_f16 v72, v64, v72
	v_add_f32_e32 v84, v76, v77
	v_fmac_f32_e32 v187, v123, v186
	v_exp_f32_e32 v126, v126
	v_cvt_pkrtz_f16_f32 v73, v186, v187
	v_fmac_f32_e32 v188, v124, v187
	v_pk_mul_f16 v73, v65, v73
	v_add_f32_e32 v85, v78, v79
	v_fmac_f32_e32 v189, v125, v188
	v_exp_f32_e32 v127, v127
	v_cvt_pkrtz_f16_f32 v74, v188, v189
	v_fmac_f32_e32 v190, v126, v189
	v_add_f32_e32 v84, v84, v85
	v_fmac_f32_e32 v191, v127, v190
	v_pk_mul_f16 v74, v66, v74
	v_cvt_pkrtz_f16_f32 v75, v190, v191
	v_mfma_f32_16x16x4_f32 a[8:11], v84, v15, 0
	v_pk_mul_f16 v75, v67, v75
	v_exp_f32_e32 v96, v96
	v_exp_f32_e32 v97, v97
	v_mfma_f32_16x16x32_f16 v[80:83], v[72:75], v[24:27], v[80:83]
	ds_read_b128 v[60:63], v2 offset:43008
	s_waitcnt lgkmcnt(1)
	v_exp_f32_e32 v98, v98
	v_exp_f32_e32 v99, v99
	v_mfma_f32_32x32x16_f16 v[112:127], v[32:35], v[28:31], 0
	ds_read_u16 v32, v9 offset:192
	ds_read_b128 v[64:67], v2 offset:44032
	v_fmac_f32_e32 v128, v96, v191
	v_exp_f32_e32 v100, v100
	v_fmac_f32_e32 v129, v97, v128
	v_exp_f32_e32 v101, v101
	v_fmac_f32_e32 v130, v98, v129
	v_cvt_pkrtz_f16_f32 v68, v128, v129
	v_exp_f32_e32 v102, v102
	v_fmac_f32_e32 v131, v99, v130
	v_pk_mul_f16 v68, v52, v68
	v_exp_f32_e32 v103, v103
	v_mfma_f32_32x32x16_f16 v[144:159], v[36:39], v[44:47], 0
	ds_read_b128 v[44:47], v2 offset:12288
	v_fmac_f32_e32 v132, v100, v131
	v_cvt_pkrtz_f16_f32 v69, v130, v131
	v_exp_f32_e32 v104, v104
	v_fmac_f32_e32 v133, v101, v132
	v_pk_mul_f16 v69, v53, v69
	v_exp_f32_e32 v105, v105
	v_fmac_f32_e32 v134, v102, v133
	v_cvt_pkrtz_f16_f32 v70, v132, v133
	v_exp_f32_e32 v106, v106
	v_fmac_f32_e32 v135, v103, v134
	v_pk_mul_f16 v70, v54, v70
	v_exp_f32_e32 v107, v107
	v_mfma_f32_32x32x16_f16 v[176:191], v[36:39], v[48:51], 0
	ds_read_b128 v[36:39], v11 offset:1536
	ds_read_b128 v[48:51], v2 offset:13312
	v_cvt_pkrtz_f16_f32 v71, v134, v135
	v_fmac_f32_e32 v168, v104, v135
	v_pk_mul_f16 v71, v55, v71
	v_exp_f32_e32 v108, v108
	v_fmac_f32_e32 v169, v105, v168
	v_mfma_f32_16x16x32_f16 v[76:79], v[68:71], v[20:23], 0
	v_cvt_pkrtz_f16_f32 v72, v168, v169
	v_exp_f32_e32 v109, v109
	v_fmac_f32_e32 v170, v106, v169
	v_pk_mul_f16 v72, v56, v72
	v_add_f32_e32 v84, v80, v81
	v_fmac_f32_e32 v171, v107, v170
	v_exp_f32_e32 v110, v110
	v_cvt_pkrtz_f16_f32 v73, v170, v171
	v_fmac_f32_e32 v172, v108, v171
	v_pk_mul_f16 v73, v57, v73
	v_add_f32_e32 v85, v82, v83
	v_fmac_f32_e32 v173, v109, v172
	v_exp_f32_e32 v111, v111
	v_cvt_pkrtz_f16_f32 v74, v172, v173
	v_fmac_f32_e32 v174, v110, v173
	v_add_f32_e32 v84, v84, v85
	v_fmac_f32_e32 v175, v111, v174
	v_pk_mul_f16 v74, v58, v74
	v_cvt_pkrtz_f16_f32 v75, v174, v175
	v_mfma_f32_16x16x4_f32 a[12:15], v84, v15, 0
	v_pk_mul_f16 v75, v59, v75
	v_exp_f32_e32 v112, v112
	v_exp_f32_e32 v113, v113
	v_mfma_f32_16x16x32_f16 v[76:79], v[72:75], v[24:27], v[76:79]
	ds_read_b128 v[52:55], v2 offset:45056
	s_waitcnt lgkmcnt(1)
	v_exp_f32_e32 v114, v114
	v_exp_f32_e32 v115, v115
	v_mfma_f32_32x32x16_f16 v[96:111], v[32:35], v[28:31], 0
	ds_read_u16 v32, v9 offset:224
	ds_read_b128 v[56:59], v2 offset:46080
	v_fmac_f32_e32 v144, v112, v175
	v_exp_f32_e32 v116, v116
	v_fmac_f32_e32 v145, v113, v144
	v_exp_f32_e32 v117, v117
	v_fmac_f32_e32 v146, v114, v145
	v_cvt_pkrtz_f16_f32 v68, v144, v145
	v_exp_f32_e32 v118, v118
	v_fmac_f32_e32 v147, v115, v146
	v_pk_mul_f16 v68, v60, v68
	v_exp_f32_e32 v119, v119
	v_mfma_f32_32x32x16_f16 v[128:143], v[36:39], v[44:47], 0
	ds_read_b128 v[44:47], v2 offset:14336
	v_fmac_f32_e32 v148, v116, v147
	v_cvt_pkrtz_f16_f32 v69, v146, v147
	v_exp_f32_e32 v120, v120
	v_fmac_f32_e32 v149, v117, v148
	v_pk_mul_f16 v69, v61, v69
	v_exp_f32_e32 v121, v121
	v_fmac_f32_e32 v150, v118, v149
	v_cvt_pkrtz_f16_f32 v70, v148, v149
	v_exp_f32_e32 v122, v122
	v_fmac_f32_e32 v151, v119, v150
	v_pk_mul_f16 v70, v62, v70
	v_exp_f32_e32 v123, v123
	v_mfma_f32_32x32x16_f16 v[160:175], v[36:39], v[48:51], 0
	ds_read_b128 v[36:39], v11 offset:1792
	ds_read_b128 v[48:51], v2 offset:15360
	v_cvt_pkrtz_f16_f32 v71, v150, v151
	v_fmac_f32_e32 v184, v120, v151
	v_pk_mul_f16 v71, v63, v71
	v_exp_f32_e32 v124, v124
	v_fmac_f32_e32 v185, v121, v184
	v_mfma_f32_16x16x32_f16 v[80:83], v[68:71], v[20:23], 0
	v_cvt_pkrtz_f16_f32 v72, v184, v185
	v_exp_f32_e32 v125, v125
	v_fmac_f32_e32 v186, v122, v185
	v_pk_mul_f16 v72, v64, v72
	v_add_f32_e32 v84, v76, v77
	v_fmac_f32_e32 v187, v123, v186
	v_exp_f32_e32 v126, v126
	v_cvt_pkrtz_f16_f32 v73, v186, v187
	v_fmac_f32_e32 v188, v124, v187
	v_pk_mul_f16 v73, v65, v73
	v_add_f32_e32 v85, v78, v79
	v_fmac_f32_e32 v189, v125, v188
	v_exp_f32_e32 v127, v127
	v_cvt_pkrtz_f16_f32 v74, v188, v189
	v_fmac_f32_e32 v190, v126, v189
	v_add_f32_e32 v84, v84, v85
	v_fmac_f32_e32 v191, v127, v190
	v_pk_mul_f16 v74, v66, v74
	v_cvt_pkrtz_f16_f32 v75, v190, v191
	v_mfma_f32_16x16x4_f32 a[16:19], v84, v15, 0
	v_pk_mul_f16 v75, v67, v75
	v_exp_f32_e32 v96, v96
	v_exp_f32_e32 v97, v97
	v_mfma_f32_16x16x32_f16 v[80:83], v[72:75], v[24:27], v[80:83]
	ds_read_b128 v[60:63], v2 offset:47104
	ds_read_b128 v[64:67], v2 offset:48128
	s_waitcnt vmcnt(0)
	ds_write_b16 v8, v18 offset:2560
	ds_write_b16 v8, v19 offset:3584
	s_waitcnt lgkmcnt(0)
	s_barrier
	v_exp_f32_e32 v98, v98
	v_exp_f32_e32 v99, v99
	v_mfma_f32_32x32x16_f16 v[112:127], v[32:35], v[28:31], 0
	s_mov_b32 m0, s32
	ds_read_u16 v32, v10 offset:0
	global_load_lds_dwordx4 v2, s[20:21]
	v_fmac_f32_e32 v128, v96, v191
	v_exp_f32_e32 v100, v100
	v_fmac_f32_e32 v129, v97, v128
	v_exp_f32_e32 v101, v101
	v_fmac_f32_e32 v130, v98, v129
	v_cvt_pkrtz_f16_f32 v68, v128, v129
	v_exp_f32_e32 v102, v102
	v_fmac_f32_e32 v131, v99, v130
	v_pk_mul_f16 v68, v52, v68
	v_exp_f32_e32 v103, v103
	v_mfma_f32_32x32x16_f16 v[144:159], v[36:39], v[44:47], 0
	s_add_i32 m0, s32, 32768
	ds_read_b128 v[44:47], v2 offset:16384
	global_load_lds_dwordx4 v2, s[22:23]
	v_fmac_f32_e32 v132, v100, v131
	v_cvt_pkrtz_f16_f32 v69, v130, v131
	v_exp_f32_e32 v104, v104
	v_fmac_f32_e32 v133, v101, v132
	v_pk_mul_f16 v69, v53, v69
	v_exp_f32_e32 v105, v105
	v_fmac_f32_e32 v134, v102, v133
	v_cvt_pkrtz_f16_f32 v70, v132, v133
	v_exp_f32_e32 v106, v106
	v_fmac_f32_e32 v135, v103, v134
	v_pk_mul_f16 v70, v54, v70
	v_exp_f32_e32 v107, v107
	v_mfma_f32_32x32x16_f16 v[176:191], v[36:39], v[48:51], 0
	ds_read_b128 v[36:39], v13 offset:0
	s_mov_b32 m0, s33
	ds_read_b128 v[48:51], v2 offset:17408
	global_load_lds_dwordx4 v3, s[20:21]
	v_cvt_pkrtz_f16_f32 v71, v134, v135
	v_fmac_f32_e32 v168, v104, v135
	v_pk_mul_f16 v71, v55, v71
	v_exp_f32_e32 v108, v108
	v_fmac_f32_e32 v169, v105, v168
	v_mfma_f32_16x16x32_f16 v[76:79], v[68:71], v[20:23], 0
	s_cmp_eq_u32 s40, 0
	s_cselect_b64 s[56:57], 0, s[42:43]
	s_and_saveexec_b64 s[44:45], s[56:57]
	global_store_dwordx4 v[16:17], a[20:23], off offset:-192
	global_store_dwordx4 v[16:17], a[24:27], off offset:-128
	global_store_dwordx4 v[16:17], a[28:31], off offset:-64
	s_and_b64 exec, s[44:45], s[42:43]
	global_store_dwordx4 v[16:17], a[0:3], off
	global_store_dwordx4 v[16:17], a[4:7], off offset:64
	global_store_dwordx4 v[16:17], a[8:11], off offset:128
	global_store_dwordx4 v[16:17], a[12:15], off offset:192
	global_store_dwordx4 v[16:17], a[16:19], off offset:256
	s_mov_b64 exec, s[44:45]
	v_cvt_pkrtz_f16_f32 v72, v168, v169
	v_exp_f32_e32 v109, v109
	v_fmac_f32_e32 v170, v106, v169
	v_pk_mul_f16 v72, v56, v72
	v_add_f32_e32 v84, v80, v81
	v_fmac_f32_e32 v171, v107, v170
	v_exp_f32_e32 v110, v110
	v_cvt_pkrtz_f16_f32 v73, v170, v171
	v_fmac_f32_e32 v172, v108, v171
	v_pk_mul_f16 v73, v57, v73
	v_add_f32_e32 v85, v82, v83
	v_fmac_f32_e32 v173, v109, v172
	v_exp_f32_e32 v111, v111
	v_cvt_pkrtz_f16_f32 v74, v172, v173
	v_fmac_f32_e32 v174, v110, v173
	v_add_f32_e32 v84, v84, v85
	v_fmac_f32_e32 v175, v111, v174
	v_pk_mul_f16 v74, v58, v74
	v_cvt_pkrtz_f16_f32 v75, v174, v175
	v_mfma_f32_16x16x4_f32 a[20:23], v84, v15, 0
	s_add_i32 m0, s33, 32768
	s_nop 0
	global_load_lds_dwordx4 v3, s[22:23]
	v_pk_mul_f16 v75, v59, v75
	v_lshl_add_u64 v[16:17], v[16:17], 0, s[46:47]
	v_exp_f32_e32 v112, v112
	v_exp_f32_e32 v113, v113
	v_mfma_f32_16x16x32_f16 v[76:79], v[72:75], v[24:27], v[76:79]
	s_mov_b32 m0, s34
	ds_read_b128 v[52:55], v2 offset:49152
	global_load_lds_dwordx4 v4, s[20:21]
	s_waitcnt lgkmcnt(1)
	v_exp_f32_e32 v114, v114
	v_exp_f32_e32 v115, v115
	v_mfma_f32_32x32x16_f16 v[96:111], v[32:35], v[28:31], 0
	ds_read_u16 v32, v10 offset:32
	s_add_i32 m0, s34, 32768
	ds_read_b128 v[56:59], v2 offset:50176
	global_load_lds_dwordx4 v4, s[22:23]
	v_fmac_f32_e32 v144, v112, v175
	v_exp_f32_e32 v116, v116
	v_fmac_f32_e32 v145, v113, v144
	v_exp_f32_e32 v117, v117
	v_fmac_f32_e32 v146, v114, v145
	v_cvt_pkrtz_f16_f32 v68, v144, v145
	v_exp_f32_e32 v118, v118
	v_fmac_f32_e32 v147, v115, v146
	v_pk_mul_f16 v68, v60, v68
	v_exp_f32_e32 v119, v119
	v_mfma_f32_32x32x16_f16 v[128:143], v[36:39], v[44:47], 0
	s_mov_b32 m0, s35
	ds_read_b128 v[44:47], v2 offset:18432
	global_load_lds_dwordx4 v5, s[20:21]
	v_fmac_f32_e32 v148, v116, v147
	v_cvt_pkrtz_f16_f32 v69, v146, v147
	v_exp_f32_e32 v120, v120
	v_fmac_f32_e32 v149, v117, v148
	v_pk_mul_f16 v69, v61, v69
	v_exp_f32_e32 v121, v121
	v_fmac_f32_e32 v150, v118, v149
	v_cvt_pkrtz_f16_f32 v70, v148, v149
	v_exp_f32_e32 v122, v122
	v_fmac_f32_e32 v151, v119, v150
	v_pk_mul_f16 v70, v62, v70
	v_exp_f32_e32 v123, v123
	v_mfma_f32_32x32x16_f16 v[160:175], v[36:39], v[48:51], 0
	ds_read_b128 v[36:39], v13 offset:256
	s_add_i32 m0, s35, 32768
	ds_read_b128 v[48:51], v2 offset:19456
	global_load_lds_dwordx4 v5, s[22:23]
	v_cvt_pkrtz_f16_f32 v71, v150, v151
	v_fmac_f32_e32 v184, v120, v151
	v_pk_mul_f16 v71, v63, v71
	v_exp_f32_e32 v124, v124
	v_fmac_f32_e32 v185, v121, v184
	v_mfma_f32_16x16x32_f16 v[80:83], v[68:71], v[20:23], 0
	s_mov_b32 m0, s28
	s_nop 0
	global_load_lds_dword v6, s[24:25]
	global_load_ushort v18, v7, s[26:27]
	global_load_ushort v19, v7, s[26:27] offset:128
	v_cvt_pkrtz_f16_f32 v72, v184, v185
	v_exp_f32_e32 v125, v125
	v_fmac_f32_e32 v186, v122, v185
	v_pk_mul_f16 v72, v64, v72
	v_add_f32_e32 v84, v76, v77
	v_fmac_f32_e32 v187, v123, v186
	v_exp_f32_e32 v126, v126
	v_cvt_pkrtz_f16_f32 v73, v186, v187
	v_fmac_f32_e32 v188, v124, v187
	v_pk_mul_f16 v73, v65, v73
	v_add_f32_e32 v85, v78, v79
	v_fmac_f32_e32 v189, v125, v188
	v_exp_f32_e32 v127, v127
	v_cvt_pkrtz_f16_f32 v74, v188, v189
	v_fmac_f32_e32 v190, v126, v189
	v_add_f32_e32 v84, v84, v85
	v_fmac_f32_e32 v191, v127, v190
	v_pk_mul_f16 v74, v66, v74
	v_cvt_pkrtz_f16_f32 v75, v190, v191
	v_mfma_f32_16x16x4_f32 a[24:27], v84, v15, 0
	s_cmp_lt_u32 s40, 15
	s_cselect_b32 s58, 0x4000, 0
	s_cselect_b32 s59, 0x100, 0
	s_add_u32 s20, s20, s58
	s_addc_u32 s21, s21, 0
	s_add_u32 s22, s22, s58
	s_addc_u32 s23, s23, 0
	s_add_u32 s24, s24, s59
	s_addc_u32 s25, s25, 0
	s_add_u32 s26, s26, s59
	s_addc_u32 s27, s27, 0
	v_pk_mul_f16 v75, v67, v75
	v_exp_f32_e32 v96, v96
	v_exp_f32_e32 v97, v97
	v_mfma_f32_16x16x32_f16 v[80:83], v[72:75], v[24:27], v[80:83]
	ds_read_b128 v[60:63], v2 offset:51200
	s_waitcnt lgkmcnt(1)
	v_exp_f32_e32 v98, v98
	v_exp_f32_e32 v99, v99
	v_mfma_f32_32x32x16_f16 v[112:127], v[32:35], v[28:31], 0
	ds_read_u16 v32, v10 offset:64
	ds_read_b128 v[64:67], v2 offset:52224
	v_fmac_f32_e32 v128, v96, v191
	v_exp_f32_e32 v100, v100
	v_fmac_f32_e32 v129, v97, v128
	v_exp_f32_e32 v101, v101
	v_fmac_f32_e32 v130, v98, v129
	v_cvt_pkrtz_f16_f32 v68, v128, v129
	v_exp_f32_e32 v102, v102
	v_fmac_f32_e32 v131, v99, v130
	v_pk_mul_f16 v68, v52, v68
	v_exp_f32_e32 v103, v103
	v_mfma_f32_32x32x16_f16 v[144:159], v[36:39], v[44:47], 0
	ds_read_b128 v[44:47], v2 offset:20480
	v_fmac_f32_e32 v132, v100, v131
	v_cvt_pkrtz_f16_f32 v69, v130, v131
	v_exp_f32_e32 v104, v104
	v_fmac_f32_e32 v133, v101, v132
	v_pk_mul_f16 v69, v53, v69
	v_exp_f32_e32 v105, v105
	v_fmac_f32_e32 v134, v102, v133
	v_cvt_pkrtz_f16_f32 v70, v132, v133
	v_exp_f32_e32 v106, v106
	v_fmac_f32_e32 v135, v103, v134
	v_pk_mul_f16 v70, v54, v70
	v_exp_f32_e32 v107, v107
	v_mfma_f32_32x32x16_f16 v[176:191], v[36:39], v[48:51], 0
	ds_read_b128 v[36:39], v13 offset:512
	ds_read_b128 v[48:51], v2 offset:21504
	v_cvt_pkrtz_f16_f32 v71, v134, v135
	v_fmac_f32_e32 v168, v104, v135
	v_pk_mul_f16 v71, v55, v71
	v_exp_f32_e32 v108, v108
	v_fmac_f32_e32 v169, v105, v168
	v_mfma_f32_16x16x32_f16 v[76:79], v[68:71], v[20:23], 0
	v_cvt_pkrtz_f16_f32 v72, v168, v169
	v_exp_f32_e32 v109, v109
	v_fmac_f32_e32 v170, v106, v169
	v_pk_mul_f16 v72, v56, v72
	v_add_f32_e32 v84, v80, v81
	v_fmac_f32_e32 v171, v107, v170
	v_exp_f32_e32 v110, v110
	v_cvt_pkrtz_f16_f32 v73, v170, v171
	v_fmac_f32_e32 v172, v108, v171
	v_pk_mul_f16 v73, v57, v73
	v_add_f32_e32 v85, v82, v83
	v_fmac_f32_e32 v173, v109, v172
	v_exp_f32_e32 v111, v111
	v_cvt_pkrtz_f16_f32 v74, v172, v173
	v_fmac_f32_e32 v174, v110, v173
	v_add_f32_e32 v84, v84, v85
	v_fmac_f32_e32 v175, v111, v174
	v_pk_mul_f16 v74, v58, v74
	v_cvt_pkrtz_f16_f32 v75, v174, v175
	v_mfma_f32_16x16x4_f32 a[28:31], v84, v15, 0
	v_pk_mul_f16 v75, v59, v75
	v_exp_f32_e32 v112, v112
	v_exp_f32_e32 v113, v113
	v_mfma_f32_16x16x32_f16 v[76:79], v[72:75], v[24:27], v[76:79]
	ds_read_b128 v[52:55], v2 offset:53248
	s_waitcnt lgkmcnt(1)
	v_exp_f32_e32 v114, v114
	v_exp_f32_e32 v115, v115
	v_mfma_f32_32x32x16_f16 v[96:111], v[32:35], v[28:31], 0
	ds_read_u16 v32, v10 offset:96
	ds_read_b128 v[56:59], v2 offset:54272
	v_fmac_f32_e32 v144, v112, v175
	v_exp_f32_e32 v116, v116
	v_fmac_f32_e32 v145, v113, v144
	v_exp_f32_e32 v117, v117
	v_fmac_f32_e32 v146, v114, v145
	v_cvt_pkrtz_f16_f32 v68, v144, v145
	v_exp_f32_e32 v118, v118
	v_fmac_f32_e32 v147, v115, v146
	v_pk_mul_f16 v68, v60, v68
	v_exp_f32_e32 v119, v119
	v_mfma_f32_32x32x16_f16 v[128:143], v[36:39], v[44:47], 0
	ds_read_b128 v[44:47], v2 offset:22528
	v_fmac_f32_e32 v148, v116, v147
	v_cvt_pkrtz_f16_f32 v69, v146, v147
	v_exp_f32_e32 v120, v120
	v_fmac_f32_e32 v149, v117, v148
	v_pk_mul_f16 v69, v61, v69
	v_exp_f32_e32 v121, v121
	v_fmac_f32_e32 v150, v118, v149
	v_cvt_pkrtz_f16_f32 v70, v148, v149
	v_exp_f32_e32 v122, v122
	v_fmac_f32_e32 v151, v119, v150
	v_pk_mul_f16 v70, v62, v70
	v_exp_f32_e32 v123, v123
	v_mfma_f32_32x32x16_f16 v[160:175], v[36:39], v[48:51], 0
	ds_read_b128 v[36:39], v13 offset:768
	ds_read_b128 v[48:51], v2 offset:23552
	v_cvt_pkrtz_f16_f32 v71, v150, v151
	v_fmac_f32_e32 v184, v120, v151
	v_pk_mul_f16 v71, v63, v71
	v_exp_f32_e32 v124, v124
	v_fmac_f32_e32 v185, v121, v184
	v_mfma_f32_16x16x32_f16 v[80:83], v[68:71], v[20:23], 0
	v_cvt_pkrtz_f16_f32 v72, v184, v185
	v_exp_f32_e32 v125, v125
	v_fmac_f32_e32 v186, v122, v185
	v_pk_mul_f16 v72, v64, v72
	v_add_f32_e32 v84, v76, v77
	v_fmac_f32_e32 v187, v123, v186
	v_exp_f32_e32 v126, v126
	v_cvt_pkrtz_f16_f32 v73, v186, v187
	v_fmac_f32_e32 v188, v124, v187
	v_pk_mul_f16 v73, v65, v73
	v_add_f32_e32 v85, v78, v79
	v_fmac_f32_e32 v189, v125, v188
	v_exp_f32_e32 v127, v127
	v_cvt_pkrtz_f16_f32 v74, v188, v189
	v_fmac_f32_e32 v190, v126, v189
	v_add_f32_e32 v84, v84, v85
	v_fmac_f32_e32 v191, v127, v190
	v_pk_mul_f16 v74, v66, v74
	v_cvt_pkrtz_f16_f32 v75, v190, v191
	v_mfma_f32_16x16x4_f32 a[0:3], v84, v15, 0
	v_pk_mul_f16 v75, v67, v75
	v_exp_f32_e32 v96, v96
	v_exp_f32_e32 v97, v97
	v_mfma_f32_16x16x32_f16 v[80:83], v[72:75], v[24:27], v[80:83]
	ds_read_b128 v[60:63], v2 offset:55296
	s_waitcnt lgkmcnt(1)
	v_exp_f32_e32 v98, v98
	v_exp_f32_e32 v99, v99
	v_mfma_f32_32x32x16_f16 v[112:127], v[32:35], v[28:31], 0
	ds_read_u16 v32, v10 offset:128
	ds_read_b128 v[64:67], v2 offset:56320
	v_fmac_f32_e32 v128, v96, v191
	v_exp_f32_e32 v100, v100
	v_fmac_f32_e32 v129, v97, v128
	v_exp_f32_e32 v101, v101
	v_fmac_f32_e32 v130, v98, v129
	v_cvt_pkrtz_f16_f32 v68, v128, v129
	v_exp_f32_e32 v102, v102
	v_fmac_f32_e32 v131, v99, v130
	v_pk_mul_f16 v68, v52, v68
	v_exp_f32_e32 v103, v103
	v_mfma_f32_32x32x16_f16 v[144:159], v[36:39], v[44:47], 0
	ds_read_b128 v[44:47], v2 offset:24576
	v_fmac_f32_e32 v132, v100, v131
	v_cvt_pkrtz_f16_f32 v69, v130, v131
	v_exp_f32_e32 v104, v104
	v_fmac_f32_e32 v133, v101, v132
	v_pk_mul_f16 v69, v53, v69
	v_exp_f32_e32 v105, v105
	v_fmac_f32_e32 v134, v102, v133
	v_cvt_pkrtz_f16_f32 v70, v132, v133
	v_exp_f32_e32 v106, v106
	v_fmac_f32_e32 v135, v103, v134
	v_pk_mul_f16 v70, v54, v70
	v_exp_f32_e32 v107, v107
	v_mfma_f32_32x32x16_f16 v[176:191], v[36:39], v[48:51], 0
	ds_read_b128 v[36:39], v13 offset:1024
	ds_read_b128 v[48:51], v2 offset:25600
	v_cvt_pkrtz_f16_f32 v71, v134, v135
	v_fmac_f32_e32 v168, v104, v135
	v_pk_mul_f16 v71, v55, v71
	v_exp_f32_e32 v108, v108
	v_fmac_f32_e32 v169, v105, v168
	v_mfma_f32_16x16x32_f16 v[76:79], v[68:71], v[20:23], 0
	v_cvt_pkrtz_f16_f32 v72, v168, v169
	v_exp_f32_e32 v109, v109
	v_fmac_f32_e32 v170, v106, v169
	v_pk_mul_f16 v72, v56, v72
	v_add_f32_e32 v84, v80, v81
	v_fmac_f32_e32 v171, v107, v170
	v_exp_f32_e32 v110, v110
	v_cvt_pkrtz_f16_f32 v73, v170, v171
	v_fmac_f32_e32 v172, v108, v171
	v_pk_mul_f16 v73, v57, v73
	v_add_f32_e32 v85, v82, v83
	v_fmac_f32_e32 v173, v109, v172
	v_exp_f32_e32 v111, v111
	v_cvt_pkrtz_f16_f32 v74, v172, v173
	v_fmac_f32_e32 v174, v110, v173
	v_add_f32_e32 v84, v84, v85
	v_fmac_f32_e32 v175, v111, v174
	v_pk_mul_f16 v74, v58, v74
	v_cvt_pkrtz_f16_f32 v75, v174, v175
	v_mfma_f32_16x16x4_f32 a[4:7], v84, v15, 0
	v_pk_mul_f16 v75, v59, v75
	v_exp_f32_e32 v112, v112
	v_exp_f32_e32 v113, v113
	v_mfma_f32_16x16x32_f16 v[76:79], v[72:75], v[24:27], v[76:79]
	ds_read_b128 v[52:55], v2 offset:57344
	s_waitcnt lgkmcnt(1)
	v_exp_f32_e32 v114, v114
	v_exp_f32_e32 v115, v115
	v_mfma_f32_32x32x16_f16 v[96:111], v[32:35], v[28:31], 0
	ds_read_u16 v32, v10 offset:160
	ds_read_b128 v[56:59], v2 offset:58368
	v_fmac_f32_e32 v144, v112, v175
	v_exp_f32_e32 v116, v116
	v_fmac_f32_e32 v145, v113, v144
	v_exp_f32_e32 v117, v117
	v_fmac_f32_e32 v146, v114, v145
	v_cvt_pkrtz_f16_f32 v68, v144, v145
	v_exp_f32_e32 v118, v118
	v_fmac_f32_e32 v147, v115, v146
	v_pk_mul_f16 v68, v60, v68
	v_exp_f32_e32 v119, v119
	v_mfma_f32_32x32x16_f16 v[128:143], v[36:39], v[44:47], 0
	ds_read_b128 v[44:47], v2 offset:26624
	v_fmac_f32_e32 v148, v116, v147
	v_cvt_pkrtz_f16_f32 v69, v146, v147
	v_exp_f32_e32 v120, v120
	v_fmac_f32_e32 v149, v117, v148
	v_pk_mul_f16 v69, v61, v69
	v_exp_f32_e32 v121, v121
	v_fmac_f32_e32 v150, v118, v149
	v_cvt_pkrtz_f16_f32 v70, v148, v149
	v_exp_f32_e32 v122, v122
	v_fmac_f32_e32 v151, v119, v150
	v_pk_mul_f16 v70, v62, v70
	v_exp_f32_e32 v123, v123
	v_mfma_f32_32x32x16_f16 v[160:175], v[36:39], v[48:51], 0
	ds_read_b128 v[36:39], v13 offset:1280
	ds_read_b128 v[48:51], v2 offset:27648
	v_cvt_pkrtz_f16_f32 v71, v150, v151
	v_fmac_f32_e32 v184, v120, v151
	v_pk_mul_f16 v71, v63, v71
	v_exp_f32_e32 v124, v124
	v_fmac_f32_e32 v185, v121, v184
	v_mfma_f32_16x16x32_f16 v[80:83], v[68:71], v[20:23], 0
	v_cvt_pkrtz_f16_f32 v72, v184, v185
	v_exp_f32_e32 v125, v125
	v_fmac_f32_e32 v186, v122, v185
	v_pk_mul_f16 v72, v64, v72
	v_add_f32_e32 v84, v76, v77
	v_fmac_f32_e32 v187, v123, v186
	v_exp_f32_e32 v126, v126
	v_cvt_pkrtz_f16_f32 v73, v186, v187
	v_fmac_f32_e32 v188, v124, v187
	v_pk_mul_f16 v73, v65, v73
	v_add_f32_e32 v85, v78, v79
	v_fmac_f32_e32 v189, v125, v188
	v_exp_f32_e32 v127, v127
	v_cvt_pkrtz_f16_f32 v74, v188, v189
	v_fmac_f32_e32 v190, v126, v189
	v_add_f32_e32 v84, v84, v85
	v_fmac_f32_e32 v191, v127, v190
	v_pk_mul_f16 v74, v66, v74
	v_cvt_pkrtz_f16_f32 v75, v190, v191
	v_mfma_f32_16x16x4_f32 a[8:11], v84, v15, 0
	v_pk_mul_f16 v75, v67, v75
	v_exp_f32_e32 v96, v96
	v_exp_f32_e32 v97, v97
	v_mfma_f32_16x16x32_f16 v[80:83], v[72:75], v[24:27], v[80:83]
	ds_read_b128 v[60:63], v2 offset:59392
	s_waitcnt lgkmcnt(1)
	v_exp_f32_e32 v98, v98
	v_exp_f32_e32 v99, v99
	v_mfma_f32_32x32x16_f16 v[112:127], v[32:35], v[28:31], 0
	ds_read_u16 v32, v10 offset:192
	ds_read_b128 v[64:67], v2 offset:60416
	v_fmac_f32_e32 v128, v96, v191
	v_exp_f32_e32 v100, v100
	v_fmac_f32_e32 v129, v97, v128
	v_exp_f32_e32 v101, v101
	v_fmac_f32_e32 v130, v98, v129
	v_cvt_pkrtz_f16_f32 v68, v128, v129
	v_exp_f32_e32 v102, v102
	v_fmac_f32_e32 v131, v99, v130
	v_pk_mul_f16 v68, v52, v68
	v_exp_f32_e32 v103, v103
	v_mfma_f32_32x32x16_f16 v[144:159], v[36:39], v[44:47], 0
	ds_read_b128 v[44:47], v2 offset:28672
	v_fmac_f32_e32 v132, v100, v131
	v_cvt_pkrtz_f16_f32 v69, v130, v131
	v_exp_f32_e32 v104, v104
	v_fmac_f32_e32 v133, v101, v132
	v_pk_mul_f16 v69, v53, v69
	v_exp_f32_e32 v105, v105
	v_fmac_f32_e32 v134, v102, v133
	v_cvt_pkrtz_f16_f32 v70, v132, v133
	v_exp_f32_e32 v106, v106
	v_fmac_f32_e32 v135, v103, v134
	v_pk_mul_f16 v70, v54, v70
	v_exp_f32_e32 v107, v107
	v_mfma_f32_32x32x16_f16 v[176:191], v[36:39], v[48:51], 0
	ds_read_b128 v[36:39], v13 offset:1536
	ds_read_b128 v[48:51], v2 offset:29696
	v_cvt_pkrtz_f16_f32 v71, v134, v135
	v_fmac_f32_e32 v168, v104, v135
	v_pk_mul_f16 v71, v55, v71
	v_exp_f32_e32 v108, v108
	v_fmac_f32_e32 v169, v105, v168
	v_mfma_f32_16x16x32_f16 v[76:79], v[68:71], v[20:23], 0
	v_cvt_pkrtz_f16_f32 v72, v168, v169
	v_exp_f32_e32 v109, v109
	v_fmac_f32_e32 v170, v106, v169
	v_pk_mul_f16 v72, v56, v72
	v_add_f32_e32 v84, v80, v81
	v_fmac_f32_e32 v171, v107, v170
	v_exp_f32_e32 v110, v110
	v_cvt_pkrtz_f16_f32 v73, v170, v171
	v_fmac_f32_e32 v172, v108, v171
	v_pk_mul_f16 v73, v57, v73
	v_add_f32_e32 v85, v82, v83
	v_fmac_f32_e32 v173, v109, v172
	v_exp_f32_e32 v111, v111
	v_cvt_pkrtz_f16_f32 v74, v172, v173
	v_fmac_f32_e32 v174, v110, v173
	v_add_f32_e32 v84, v84, v85
	v_fmac_f32_e32 v175, v111, v174
	v_pk_mul_f16 v74, v58, v74
	v_cvt_pkrtz_f16_f32 v75, v174, v175
	v_mfma_f32_16x16x4_f32 a[12:15], v84, v15, 0
	v_pk_mul_f16 v75, v59, v75
	v_exp_f32_e32 v112, v112
	v_exp_f32_e32 v113, v113
	v_mfma_f32_16x16x32_f16 v[76:79], v[72:75], v[24:27], v[76:79]
	ds_read_b128 v[52:55], v2 offset:61440
	s_waitcnt lgkmcnt(1)
	v_exp_f32_e32 v114, v114
	v_exp_f32_e32 v115, v115
	v_mfma_f32_32x32x16_f16 v[96:111], v[32:35], v[28:31], 0
	ds_read_u16 v32, v10 offset:224
	ds_read_b128 v[56:59], v2 offset:62464
	v_fmac_f32_e32 v144, v112, v175
	v_exp_f32_e32 v116, v116
	v_fmac_f32_e32 v145, v113, v144
	v_exp_f32_e32 v117, v117
	v_fmac_f32_e32 v146, v114, v145
	v_cvt_pkrtz_f16_f32 v68, v144, v145
	v_exp_f32_e32 v118, v118
	v_fmac_f32_e32 v147, v115, v146
	v_pk_mul_f16 v68, v60, v68
	v_exp_f32_e32 v119, v119
	v_mfma_f32_32x32x16_f16 v[128:143], v[36:39], v[44:47], 0
	ds_read_b128 v[44:47], v2 offset:30720
	v_fmac_f32_e32 v148, v116, v147
	v_cvt_pkrtz_f16_f32 v69, v146, v147
	v_exp_f32_e32 v120, v120
	v_fmac_f32_e32 v149, v117, v148
	v_pk_mul_f16 v69, v61, v69
	v_exp_f32_e32 v121, v121
	v_fmac_f32_e32 v150, v118, v149
	v_cvt_pkrtz_f16_f32 v70, v148, v149
	v_exp_f32_e32 v122, v122
	v_fmac_f32_e32 v151, v119, v150
	v_pk_mul_f16 v70, v62, v70
	v_exp_f32_e32 v123, v123
	v_mfma_f32_32x32x16_f16 v[160:175], v[36:39], v[48:51], 0
	ds_read_b128 v[36:39], v13 offset:1792
	ds_read_b128 v[48:51], v2 offset:31744
	v_cvt_pkrtz_f16_f32 v71, v150, v151
	v_fmac_f32_e32 v184, v120, v151
	v_pk_mul_f16 v71, v63, v71
	v_exp_f32_e32 v124, v124
	v_fmac_f32_e32 v185, v121, v184
	v_mfma_f32_16x16x32_f16 v[80:83], v[68:71], v[20:23], 0
	v_cvt_pkrtz_f16_f32 v72, v184, v185
	v_exp_f32_e32 v125, v125
	v_fmac_f32_e32 v186, v122, v185
	v_pk_mul_f16 v72, v64, v72
	v_add_f32_e32 v84, v76, v77
	v_fmac_f32_e32 v187, v123, v186
	v_exp_f32_e32 v126, v126
	v_cvt_pkrtz_f16_f32 v73, v186, v187
	v_fmac_f32_e32 v188, v124, v187
	v_pk_mul_f16 v73, v65, v73
	v_add_f32_e32 v85, v78, v79
	v_fmac_f32_e32 v189, v125, v188
	v_exp_f32_e32 v127, v127
	v_cvt_pkrtz_f16_f32 v74, v188, v189
	v_fmac_f32_e32 v190, v126, v189
	v_add_f32_e32 v84, v84, v85
	v_fmac_f32_e32 v191, v127, v190
	v_pk_mul_f16 v74, v66, v74
	v_cvt_pkrtz_f16_f32 v75, v190, v191
	v_mfma_f32_16x16x4_f32 a[16:19], v84, v15, 0
	v_pk_mul_f16 v75, v67, v75
	v_exp_f32_e32 v96, v96
	v_exp_f32_e32 v97, v97
	v_mfma_f32_16x16x32_f16 v[80:83], v[72:75], v[24:27], v[80:83]
	ds_read_b128 v[60:63], v2 offset:63488
	ds_read_b128 v[64:67], v2 offset:64512
	s_waitcnt vmcnt(0)
	ds_write_b16 v8, v18 offset:512
	ds_write_b16 v8, v19 offset:1536
	s_waitcnt lgkmcnt(0)
	s_barrier
	v_exp_f32_e32 v98, v98
	v_exp_f32_e32 v99, v99
	v_mfma_f32_32x32x16_f16 v[112:127], v[32:35], v[28:31], 0
	s_add_i32 m0, s32, 16384
	ds_read_u16 v32, v9 offset:0
	global_load_lds_dwordx4 v2, s[20:21]
	v_fmac_f32_e32 v128, v96, v191
	v_exp_f32_e32 v100, v100
	v_fmac_f32_e32 v129, v97, v128
	v_exp_f32_e32 v101, v101
	v_fmac_f32_e32 v130, v98, v129
	v_cvt_pkrtz_f16_f32 v68, v128, v129
	v_exp_f32_e32 v102, v102
	v_fmac_f32_e32 v131, v99, v130
	v_pk_mul_f16 v68, v52, v68
	v_exp_f32_e32 v103, v103
	v_mfma_f32_32x32x16_f16 v[144:159], v[36:39], v[44:47], 0
	s_add_i32 m0, s32, 49152
	ds_read_b128 v[44:47], v2 offset:0
	global_load_lds_dwordx4 v2, s[22:23]
	v_fmac_f32_e32 v132, v100, v131
	v_cvt_pkrtz_f16_f32 v69, v130, v131
	v_exp_f32_e32 v104, v104
	v_fmac_f32_e32 v133, v101, v132
	v_pk_mul_f16 v69, v53, v69
	v_exp_f32_e32 v105, v105
	v_fmac_f32_e32 v134, v102, v133
	v_cvt_pkrtz_f16_f32 v70, v132, v133
	v_exp_f32_e32 v106, v106
	v_fmac_f32_e32 v135, v103, v134
	v_pk_mul_f16 v70, v54, v70
	v_exp_f32_e32 v107, v107
	v_mfma_f32_32x32x16_f16 v[176:191], v[36:39], v[48:51], 0
	ds_read_b128 v[36:39], v11 offset:0
	s_add_i32 m0, s33, 16384
	ds_read_b128 v[48:51], v2 offset:1024
	global_load_lds_dwordx4 v3, s[20:21]
	v_cvt_pkrtz_f16_f32 v71, v134, v135
	v_fmac_f32_e32 v168, v104, v135
	v_pk_mul_f16 v71, v55, v71
	v_exp_f32_e32 v108, v108
	v_fmac_f32_e32 v169, v105, v168
	v_mfma_f32_16x16x32_f16 v[76:79], v[68:71], v[20:23], 0
	s_and_saveexec_b64 s[44:45], s[42:43]
	global_store_dwordx4 v[16:17], a[20:23], off offset:-192
	global_store_dwordx4 v[16:17], a[24:27], off offset:-128
	global_store_dwordx4 v[16:17], a[28:31], off offset:-64
	global_store_dwordx4 v[16:17], a[0:3], off
	global_store_dwordx4 v[16:17], a[4:7], off offset:64
	global_store_dwordx4 v[16:17], a[8:11], off offset:128
	global_store_dwordx4 v[16:17], a[12:15], off offset:192
	global_store_dwordx4 v[16:17], a[16:19], off offset:256
	s_mov_b64 exec, s[44:45]
	v_cvt_pkrtz_f16_f32 v72, v168, v169
	v_exp_f32_e32 v109, v109
	v_fmac_f32_e32 v170, v106, v169
	v_pk_mul_f16 v72, v56, v72
	v_add_f32_e32 v84, v80, v81
	v_fmac_f32_e32 v171, v107, v170
	v_exp_f32_e32 v110, v110
	v_cvt_pkrtz_f16_f32 v73, v170, v171
	v_fmac_f32_e32 v172, v108, v171
	v_pk_mul_f16 v73, v57, v73
	v_add_f32_e32 v85, v82, v83
	v_fmac_f32_e32 v173, v109, v172
	v_exp_f32_e32 v111, v111
	v_cvt_pkrtz_f16_f32 v74, v172, v173
	v_fmac_f32_e32 v174, v110, v173
	v_add_f32_e32 v84, v84, v85
	v_fmac_f32_e32 v175, v111, v174
	v_pk_mul_f16 v74, v58, v74
	v_cvt_pkrtz_f16_f32 v75, v174, v175
	v_mfma_f32_16x16x4_f32 a[20:23], v84, v15, 0
	s_add_i32 m0, s33, 49152
	s_nop 0
	global_load_lds_dwordx4 v3, s[22:23]
	v_pk_mul_f16 v75, v59, v75
	v_lshl_add_u64 v[16:17], v[16:17], 0, s[46:47]
	v_exp_f32_e32 v112, v112
	v_exp_f32_e32 v113, v113
	v_mfma_f32_16x16x32_f16 v[76:79], v[72:75], v[24:27], v[76:79]
	s_add_i32 m0, s34, 16384
	ds_read_b128 v[52:55], v2 offset:32768
	global_load_lds_dwordx4 v4, s[20:21]
	s_waitcnt lgkmcnt(1)
	v_exp_f32_e32 v114, v114
	v_exp_f32_e32 v115, v115
	v_mfma_f32_32x32x16_f16 v[96:111], v[32:35], v[28:31], 0
	ds_read_u16 v32, v9 offset:32
	s_add_i32 m0, s34, 49152
	ds_read_b128 v[56:59], v2 offset:33792
	global_load_lds_dwordx4 v4, s[22:23]
	v_fmac_f32_e32 v144, v112, v175
	v_exp_f32_e32 v116, v116
	v_fmac_f32_e32 v145, v113, v144
	v_exp_f32_e32 v117, v117
	v_fmac_f32_e32 v146, v114, v145
	v_cvt_pkrtz_f16_f32 v68, v144, v145
	v_exp_f32_e32 v118, v118
	v_fmac_f32_e32 v147, v115, v146
	v_pk_mul_f16 v68, v60, v68
	v_exp_f32_e32 v119, v119
	v_mfma_f32_32x32x16_f16 v[128:143], v[36:39], v[44:47], 0
	s_add_i32 m0, s35, 16384
	ds_read_b128 v[44:47], v2 offset:2048
	global_load_lds_dwordx4 v5, s[20:21]
	v_fmac_f32_e32 v148, v116, v147
	v_cvt_pkrtz_f16_f32 v69, v146, v147
	v_exp_f32_e32 v120, v120
	v_fmac_f32_e32 v149, v117, v148
	v_pk_mul_f16 v69, v61, v69
	v_exp_f32_e32 v121, v121
	v_fmac_f32_e32 v150, v118, v149
	v_cvt_pkrtz_f16_f32 v70, v148, v149
	v_exp_f32_e32 v122, v122
	v_fmac_f32_e32 v151, v119, v150
	v_pk_mul_f16 v70, v62, v70
	v_exp_f32_e32 v123, v123
	v_mfma_f32_32x32x16_f16 v[160:175], v[36:39], v[48:51], 0
	ds_read_b128 v[36:39], v11 offset:256
	s_add_i32 m0, s35, 49152
	ds_read_b128 v[48:51], v2 offset:3072
	global_load_lds_dwordx4 v5, s[22:23]
	v_cvt_pkrtz_f16_f32 v71, v150, v151
	v_fmac_f32_e32 v184, v120, v151
	v_pk_mul_f16 v71, v63, v71
	v_exp_f32_e32 v124, v124
	v_fmac_f32_e32 v185, v121, v184
	v_mfma_f32_16x16x32_f16 v[80:83], v[68:71], v[20:23], 0
	s_add_i32 m0, s28, 0x100
	s_nop 0
	global_load_lds_dword v6, s[24:25]
	global_load_ushort v18, v7, s[26:27]
	global_load_ushort v19, v7, s[26:27] offset:128
	v_cvt_pkrtz_f16_f32 v72, v184, v185
	v_exp_f32_e32 v125, v125
	v_fmac_f32_e32 v186, v122, v185
	v_pk_mul_f16 v72, v64, v72
	v_add_f32_e32 v84, v76, v77
	v_fmac_f32_e32 v187, v123, v186
	v_exp_f32_e32 v126, v126
	v_cvt_pkrtz_f16_f32 v73, v186, v187
	v_fmac_f32_e32 v188, v124, v187
	v_pk_mul_f16 v73, v65, v73
	v_add_f32_e32 v85, v78, v79
	v_fmac_f32_e32 v189, v125, v188
	v_exp_f32_e32 v127, v127
	v_cvt_pkrtz_f16_f32 v74, v188, v189
	v_fmac_f32_e32 v190, v126, v189
	v_add_f32_e32 v84, v84, v85
	v_fmac_f32_e32 v191, v127, v190
	v_pk_mul_f16 v74, v66, v74
	v_cvt_pkrtz_f16_f32 v75, v190, v191
	v_mfma_f32_16x16x4_f32 a[24:27], v84, v15, 0
	s_cmp_lt_u32 s40, 14
	s_cselect_b32 s58, 0x4000, 0
	s_cselect_b32 s59, 0x100, 0
	s_add_u32 s20, s20, s58
	s_addc_u32 s21, s21, 0
	s_add_u32 s22, s22, s58
	s_addc_u32 s23, s23, 0
	s_add_u32 s24, s24, s59
	s_addc_u32 s25, s25, 0
	s_add_u32 s26, s26, s59
	s_addc_u32 s27, s27, 0
	v_pk_mul_f16 v75, v67, v75
	s_add_u32 s40, s40, 1
	s_cmp_lt_u32 s40, 16
	s_cbranch_scc1 .Lscan_loop
	s_nop 1
	v_mfma_f32_16x16x32_f16 v[80:83], v[72:75], v[24:27], v[80:83]
	s_nop 15
	v_add_f32_e32 v84, v80, v81
	v_add_f32_e32 v85, v82, v83
	s_nop 0
	v_add_f32_e32 v84, v84, v85
	s_nop 1
	v_mfma_f32_16x16x4_f32 a[28:31], v84, v15, 0
	s_nop 15
	s_nop 3
	s_and_saveexec_b64 s[44:45], s[42:43]
	global_store_dwordx4 v[16:17], a[20:23], off offset:-192
	global_store_dwordx4 v[16:17], a[24:27], off offset:-128
	global_store_dwordx4 v[16:17], a[28:31], off offset:-64
	s_waitcnt vmcnt(0)
	s_endpgm
